# localsort table staging batched; L1/L2 epilogue bias+Wout from LDS (no serialized flat loads); prologue/k_prep load batching
# speedup vs baseline: 1.0692x; 1.0377x over previous
.LBB0_3:
	s_mov_b32 s2, 0xffff
	v_cmp_lt_u32_e32 vcc, s2, v14
	s_and_saveexec_b64 s[2:3], vcc
	s_xor_b64 s[2:3], exec, s[2:3]
	s_cbranch_execz .LBB0_25
	s_mov_b32 s4, 0xfffeff80
	v_cmp_gt_u32_e32 vcc, s4, v2
	s_and_saveexec_b64 s[4:5], vcc
	s_xor_b64 s[10:11], exec, s[4:5]
	s_cbranch_execz .LBB0_22
	s_mov_b32 s4, 0x1101f
	v_cmp_lt_u32_e32 vcc, s4, v14
	s_and_saveexec_b64 s[4:5], vcc
	s_xor_b64 s[12:13], exec, s[4:5]
	s_cbranch_execz .LBB0_15
	s_mov_b32 s4, 0x19258
	v_cmp_gt_u32_e32 vcc, s4, v14
	s_and_saveexec_b64 s[14:15], vcc
	s_cbranch_execz .LBB0_14
	s_load_dwordx4 s[4:7], s[0:1], 0x0
	s_load_dwordx2 s[16:17], s[0:1], 0x90
	v_add_u32_e32 v0, 0xfffff060, v2
	v_lshl_add_u32 v2, v0, 1, v0
	v_lshlrev_b32_e32 v3, 2, v2
	v_mov_b32_e32 v5, 0
	v_mov_b32_e32 v6, 0
	v_mov_b32_e32 v7, 0
	v_mov_b32_e32 v8, 0
	v_mov_b32_e32 v9, 0
	v_mov_b32_e32 v10, 0
	s_mov_b32 s18, 0x8236
	v_cmp_gt_u32_e32 vcc, s18, v0
	s_waitcnt lgkmcnt(0)
	s_and_saveexec_b64 s[18:19], vcc
	global_load_dword v5, v3, s[4:5]
	global_load_dword v6, v3, s[6:7]
	s_mov_b32 s20, 0x8235
	v_cmp_gt_u32_e32 vcc, s20, v0
	s_and_b64 exec, exec, vcc
	global_load_dword v7, v3, s[4:5] offset:4
	global_load_dword v8, v3, s[6:7] offset:4
	global_load_dword v9, v3, s[4:5] offset:8
	global_load_dword v10, v3, s[6:7] offset:8
	s_mov_b64 exec, s[18:19]
	s_waitcnt vmcnt(0)
	v_lshl_add_u32 v4, v5, 4, v6
	v_lshl_add_u32 v7, v7, 4, v8
	v_lshl_add_u32 v9, v9, 4, v10
	v_lshl_or_b32 v4, v7, 10, v4
	v_lshl_or_b32 v4, v9, 20, v4
	v_mov_b32_e32 v1, 0
	s_waitcnt lgkmcnt(0)
	v_lshl_add_u64 v[0:1], v[0:1], 2, s[16:17]
	global_store_dword v[0:1], v4, off

	.amdhsa_kernel _Z6k_prepPKiS0_PKfS2_S2_S2_S2_S2_S2_S2_S2_S2_PDF16_S3_S3_PfS4_S4_PjS3_S5_
		.amdhsa_group_segment_fixed_size 0
		.amdhsa_private_segment_fixed_size 0
		.amdhsa_kernarg_size 168
		.amdhsa_user_sgpr_count 2
		.amdhsa_user_sgpr_dispatch_ptr 0
		.amdhsa_user_sgpr_queue_ptr 0
		.amdhsa_user_sgpr_kernarg_segment_ptr 1
		.amdhsa_user_sgpr_dispatch_id 0
		.amdhsa_user_sgpr_kernarg_preload_length 0
		.amdhsa_user_sgpr_kernarg_preload_offset 0
		.amdhsa_user_sgpr_private_segment_size 0
		.amdhsa_uses_dynamic_stack 0
		.amdhsa_enable_private_segment 0
		.amdhsa_system_sgpr_workgroup_id_x 1
		.amdhsa_system_sgpr_workgroup_id_y 0
		.amdhsa_system_sgpr_workgroup_id_z 0
		.amdhsa_system_sgpr_workgroup_info 0
		.amdhsa_system_vgpr_workitem_id 0
		.amdhsa_next_free_vgpr 61
		.amdhsa_next_free_sgpr 21
		.amdhsa_accum_offset 64
		.amdhsa_reserve_vcc 1
		.amdhsa_float_round_mode_32 0
		.amdhsa_float_round_mode_16_64 0
		.amdhsa_float_denorm_mode_32 3
		.amdhsa_float_denorm_mode_16_64 3
		.amdhsa_dx10_clamp 1
		.amdhsa_ieee_mode 1
		.amdhsa_fp16_overflow 0
		.amdhsa_tg_split 0
		.amdhsa_exception_fp_ieee_invalid_op 0
		.amdhsa_exception_fp_denorm_src 0
		.amdhsa_exception_fp_ieee_div_zero 0
		.amdhsa_exception_fp_ieee_overflow 0
		.amdhsa_exception_fp_ieee_underflow 0
		.amdhsa_exception_fp_ieee_inexact 0
		.amdhsa_exception_int_div_zero 0
	.end_amdhsa_kernel

.LBB1_11:
	s_or_b64 exec, exec, s[10:11]
	v_mov_b32_e32 v35, 0
	v_add_u32_e32 v1, 0x6a0, v34
	s_waitcnt lgkmcnt(0)
	v_add_u32_e32 v76, 0x4000, v34
	v_add_u32_e32 v77, 0x8000, v34
	v_add_u32_e32 v78, 0xc000, v34
	v_add_u32_e32 v79, 0x10000, v34
	v_add_u32_e32 v80, 0x14000, v34
	v_add_u32_e32 v81, 0x18000, v34
	v_add_u32_e32 v82, 0x1c000, v34
	v_add_u32_e32 v83, 0x20000, v34
	global_load_dwordx4 v[40:43], v34, s[62:63]
	global_load_dwordx4 v[44:47], v76, s[62:63]
	global_load_dwordx4 v[48:51], v77, s[62:63]
	global_load_dwordx4 v[52:55], v78, s[62:63]
	global_load_dwordx4 v[56:59], v79, s[62:63]
	global_load_dwordx4 v[60:63], v80, s[62:63]
	global_load_dwordx4 v[64:67], v81, s[62:63]
	global_load_dwordx4 v[68:71], v82, s[62:63]
	s_movk_i32 s10, 0x8e
	s_mov_b64 s[6:7], exec
	v_cmp_gt_u32_e64 s[4:5], s10, v0
	s_and_b64 exec, exec, s[4:5]
	global_load_dwordx4 v[72:75], v83, s[62:63]
	s_mov_b64 exec, s[6:7]
	v_add_u32_e32 v84, 0x10000, v1
	v_add_u32_e32 v85, 0x20000, v1
	s_waitcnt vmcnt(0)
	ds_write_b128 v1, v[40:43]
	ds_write_b128 v1, v[44:47] offset:16384
	ds_write_b128 v1, v[48:51] offset:32768
	ds_write_b128 v1, v[52:55] offset:49152
	ds_write_b128 v84, v[56:59]
	ds_write_b128 v84, v[60:63] offset:16384
	ds_write_b128 v84, v[64:67] offset:32768
	ds_write_b128 v84, v[68:71] offset:49152
	s_and_b64 exec, exec, s[4:5]
	ds_write_b128 v85, v[72:75]
	s_mov_b64 exec, s[6:7]
	v_cmp_lt_i32_e64 s[4:5], -1, v30
	v_mov_b32_e32 v39, 0
	v_mov_b32_e32 v36, 0
	v_lshrrev_b32_e32 v37, 6, v30
	v_mov_b32_e32 v41, 0
	s_waitcnt lgkmcnt(0)
	s_barrier
	s_and_saveexec_b64 s[6:7], s[4:5]
	s_cbranch_execz .LBB1_15
	s_mov_b32 s8, 0xaaaaaaab
	v_mul_hi_u32 v39, v26, s8
	v_lshrrev_b32_e32 v39, 1, v39
	v_mov_b32_e32 v41, 0x6a0
	v_lshl_add_u32 v41, v39, 2, v41
	ds_read_b32 v44, v41
	v_mov_b32_e32 v40, 1
	v_and_b32_e32 v41, 0x3fffffc, v37
	ds_add_rtn_u32 v41, v41, v40
	v_mad_u64_u32 v[42:43], s[8:9], v39, -3, v[26:27]
	v_mul_lo_u32 v39, v42, 10
	s_waitcnt lgkmcnt(1)
	v_lshrrev_b32_e32 v39, v39, v44
	v_and_b32_e32 v39, 0x3ff, v39

_Z7k_layerILi1EEvPKDF16_PKiPKjS3_S3_S1_PKfPDF16_PhS3_S7_Pf:
	s_load_dwordx2 s[24:25], s[0:1], 0x50
	s_load_dwordx8 s[8:15], s[0:1], 0x0
	s_load_dwordx8 s[16:23], s[0:1], 0x20
	v_lshrrev_b32_e32 v2, 5, v0
	v_and_b32_e32 v4, 31, v0
	v_mul_u32_u24_e32 v3, 0x210, v2
	v_lshlrev_b32_e32 v5, 4, v4
	v_or_b32_e32 v1, 0xfffffc00, v0
	v_add3_u32 v4, v3, v5, 0
	v_lshl_or_b32 v2, v2, 9, v5
	v_mov_b32_e32 v3, 0
	s_waitcnt lgkmcnt(0)
	v_add_u32_e32 v3, 0x4000, v2
	v_lshlrev_b32_e32 v30, 4, v0
	v_cmp_gt_u32_e32 vcc, 16, v0
	s_and_saveexec_b64 s[4:5], vcc
	global_load_dwordx4 v[34:37], v30, s[20:21]
	s_mov_b64 exec, s[4:5]
	global_load_dwordx4 v[6:9], v2, s[18:19]
	global_load_dwordx4 v[10:13], v3, s[18:19]
	v_add_u32_e32 v31, 0x4000, v30
	v_add_u32_e32 v32, 0x8000, v30
	v_add_u32_e32 v33, 0xc000, v30
	global_load_dwordx4 v[14:17], v30, s[8:9]
	global_load_dwordx4 v[18:21], v31, s[8:9]
	global_load_dwordx4 v[22:25], v32, s[8:9]
	global_load_dwordx4 v[26:29], v33, s[8:9]
	v_add_u32_e32 v5, 0xcc10, v30
	s_waitcnt vmcnt(5)
	ds_write_b128 v4, v[6:9]
	s_waitcnt vmcnt(4)
	ds_write_b128 v4, v[10:13] offset:16896
	s_waitcnt vmcnt(3)
	ds_write_b128 v5, v[14:17]
	s_waitcnt vmcnt(2)
	ds_write_b128 v5, v[18:21] offset:16384
	s_waitcnt vmcnt(1)
	ds_write_b128 v5, v[22:25] offset:32768
	s_waitcnt vmcnt(0)
	ds_write_b128 v5, v[26:29] offset:49152
	v_add_u32_e32 v38, 0x1cc90, v30
	s_and_saveexec_b64 s[4:5], vcc
	ds_write_b128 v38, v[34:37]
	s_mov_b64 exec, s[4:5]
	v_cmp_gt_u32_e32 vcc, 64, v0
	s_and_saveexec_b64 s[4:5], vcc
	v_lshl_add_u32 v1, v0, 1, 0
	v_add_u32_e32 v1, 0x1cc10, v1
	v_mov_b32_e32 v2, 0
	ds_write_b16 v1, v2
	s_or_b64 exec, exec, s[4:5]
	s_mov_b32 s4, 0
	v_cmp_eq_u32_e32 vcc, 0, v0
	s_and_saveexec_b64 s[6:7], vcc
	v_mov_b32_e32 v1, 0
	ds_write_b32 v1, v1 offset:52224
	s_or_b64 exec, exec, s[6:7]
	s_waitcnt lgkmcnt(0)
	s_barrier
	s_load_dword s26, s[0:1], 0x60
	s_mul_hi_u32 s5, s2, 0x186a0
	s_cmp_lg_u64 s[4:5], 0
	s_mul_i32 s3, s2, 0x186a0
	s_waitcnt lgkmcnt(0)
	v_cvt_f32_u32_e32 v1, s26
	s_cbranch_scc0 .LBB4_104
	v_fmamk_f32 v2, 0, 0x4f800000, v1
	v_rcp_f32_e32 v2, v2
	s_sub_u32 s4, 0, s26
	s_subb_u32 s18, 0, 0
	v_mul_f32_e32 v2, 0x5f7ffffc, v2
	v_mul_f32_e32 v3, 0x2f800000, v2
	v_trunc_f32_e32 v3, v3
	v_fmamk_f32 v2, v3, 0xcf800000, v2
	v_cvt_u32_f32_e32 v3, v3
	v_cvt_u32_f32_e32 v2, v2
	v_readfirstlane_b32 s19, v3
	v_readfirstlane_b32 s8, v2
	s_mul_hi_u32 s27, s4, s8
	s_mul_i32 s28, s4, s19
	s_mul_i32 s9, s18, s8
	s_add_i32 s27, s27, s28
	s_add_i32 s27, s27, s9
	s_mul_i32 s29, s4, s8
	s_mul_i32 s28, s8, s27
	s_mul_hi_u32 s30, s8, s29
	s_mul_hi_u32 s9, s8, s27
	s_add_u32 s28, s30, s28
	s_addc_u32 s9, 0, s9
	s_mul_hi_u32 s31, s19, s29
	s_mul_i32 s29, s19, s29
	s_add_u32 s28, s28, s29
	s_mul_hi_u32 s30, s19, s27
	s_addc_u32 s9, s9, s31
	s_addc_u32 s28, s30, 0
	s_mul_i32 s27, s19, s27
	s_add_u32 s9, s9, s27
	s_addc_u32 s27, 0, s28
	s_add_u32 s28, s8, s9
	s_cselect_b64 s[8:9], -1, 0
	s_cmp_lg_u64 s[8:9], 0
	s_addc_u32 s19, s19, s27
	s_mul_i32 s8, s4, s19
	s_mul_hi_u32 s9, s4, s28
	s_add_i32 s8, s9, s8
	s_mul_i32 s18, s18, s28
	s_add_i32 s8, s8, s18
	s_mul_i32 s4, s4, s28
	s_mul_hi_u32 s18, s19, s4
	s_mul_i32 s27, s19, s4
	s_mul_i32 s30, s28, s8
	s_mul_hi_u32 s4, s28, s4
	s_mul_hi_u32 s29, s28, s8
	s_add_u32 s4, s4, s30
	s_addc_u32 s29, 0, s29
	s_add_u32 s4, s4, s27
	s_mul_hi_u32 s9, s19, s8
	s_addc_u32 s4, s29, s18
	s_addc_u32 s9, s9, 0
	s_mul_i32 s8, s19, s8
	s_add_u32 s4, s4, s8
	s_addc_u32 s18, 0, s9
	s_add_u32 s4, s28, s4
	s_cselect_b64 s[8:9], -1, 0
	s_cmp_lg_u64 s[8:9], 0
	s_addc_u32 s8, s19, s18
	s_mul_i32 s18, s3, s8
	s_mul_hi_u32 s19, s3, s4
	s_mul_hi_u32 s9, s3, s8
	s_add_u32 s18, s19, s18
	s_addc_u32 s9, 0, s9
	s_mul_hi_u32 s27, s5, s4
	s_mul_i32 s4, s5, s4
	s_add_u32 s4, s18, s4
	s_mul_hi_u32 s19, s5, s8
	s_addc_u32 s4, s9, s27
	s_addc_u32 s9, s19, 0
	s_mul_i32 s8, s5, s8
	s_add_u32 s18, s4, s8
	s_addc_u32 s4, 0, s9
	s_mul_i32 s4, s26, s4
	s_mul_hi_u32 s8, s26, s18
	s_add_u32 s19, s18, 1
	s_add_u32 s27, s18, 2
	s_add_i32 s4, s8, s4
	s_mul_i32 s8, s26, s18
	s_sub_u32 s28, s3, s8
	s_cselect_b64 s[8:9], -1, 0
	s_cmp_lg_u64 s[8:9], 0
	s_subb_u32 s8, s5, s4
	s_sub_u32 s9, s28, s26
	s_cselect_b64 s[4:5], -1, 0
	s_cmp_lg_u64 s[4:5], 0
	s_subb_u32 s4, s8, 0
	s_cmp_ge_u32 s9, s26
	s_cselect_b32 s5, -1, 0
	s_cmp_eq_u32 s4, 0
	s_cselect_b32 s4, s5, -1
	s_cmp_lg_u32 s4, 0
	s_cselect_b32 s4, s27, s19
	s_cmp_ge_u32 s28, s26
	s_cselect_b32 s5, -1, 0
	s_cmp_eq_u32 s8, 0
	s_cselect_b32 s5, s5, -1
	s_cmp_lg_u32 s5, 0
	s_cselect_b32 s8, s4, s18
	s_cbranch_execnz .LBB4_11

.LBB4_101:
	s_or_b64 exec, exec, s[6:7]
	s_waitcnt lgkmcnt(0)
	ds_write_b128 v104, v[48:51] offset:33792
	ds_read_b128 v[48:51], v105 offset:384
	ds_read_b128 v[52:55], v103 offset:33792
	ds_read_b128 v[56:59], v105 offset:8832
	s_waitcnt lgkmcnt(1)
	v_mfma_f32_16x16x32_f16 v[32:35], v[48:51], v[52:55], v[32:35]
	ds_read_b128 v[48:51], v105 offset:17280
	s_waitcnt lgkmcnt(1)
	v_mfma_f32_16x16x32_f16 v[36:39], v[56:59], v[52:55], v[36:39]
	s_waitcnt lgkmcnt(0)
	v_mfma_f32_16x16x32_f16 v[56:59], v[48:51], v[52:55], v[40:43]
	s_nop 2
	ds_read_b128 v[40:43], v105 offset:25728
	s_waitcnt lgkmcnt(0)
	v_mfma_f32_16x16x32_f16 v[50:53], v[40:43], v[52:55], v[44:47]
	ds_read_b128 v[40:43], v105 offset:448
	ds_read_b128 v[60:63], v103 offset:33856
	ds_read_b128 v[64:67], v105 offset:8896
	v_add_u32_e32 v48, s19, v99
	v_cmp_gt_i32_e32 vcc, s18, v48
	s_and_b64 s[4:5], s[2:3], vcc
	s_waitcnt lgkmcnt(1)
	v_mfma_f32_16x16x32_f16 v[44:47], v[40:43], v[60:63], v[32:35]
	s_mov_b64 s[6:7], s[20:21]
	s_mov_b64 s[22:23], s[24:25]
	s_nop 0
	ds_read_b128 v[32:35], v105 offset:17344
	s_waitcnt lgkmcnt(1)
	v_mfma_f32_16x16x32_f16 v[40:43], v[64:67], v[60:63], v[36:39]
	ds_read_b128 v[64:67], v105 offset:25792
	s_waitcnt lgkmcnt(1)
	v_mfma_f32_16x16x32_f16 v[36:39], v[32:35], v[60:63], v[56:59]
	s_waitcnt lgkmcnt(0)
	v_mfma_f32_16x16x32_f16 v[32:35], v[64:67], v[60:63], v[50:53]
	s_and_saveexec_b64 s[22:23], s[4:5]
	s_xor_b64 s[4:5], exec, s[22:23]
	s_cbranch_execz .LBB4_15
	v_add_u32_e32 v50, 0x1cc90, v88
	ds_read_b128 v[52:55], v50
	v_mov_b32_e32 v56, v89
	s_waitcnt lgkmcnt(0)
	v_add_f32_e32 v44, v44, v52
	v_add_f32_e32 v45, v45, v53
	v_max_f32_e32 v57, 0, v44
	v_max_f32_e32 v58, 0, v45
	v_mul_f32_e32 v44, 0x42800000, v57
	v_mul_f32_e32 v45, 0x42800000, v58
	v_min_f32_e32 v44, 0x43e00000, v44
	v_min_f32_e32 v45, 0x43e00000, v45
	v_add_f32_e32 v46, v46, v54
	v_add_f32_e32 v47, v47, v55
	v_cvt_pk_fp8_f32 v56, v44, v45
	v_max_f32_e32 v46, 0, v46
	v_max_f32_e32 v47, 0, v47
	v_mul_f32_e32 v49, 0x42800000, v46
	v_mul_f32_e32 v44, 0x42800000, v47
	v_min_f32_e32 v45, 0x43e00000, v49
	v_min_f32_e32 v44, 0x43e00000, v44
	v_cvt_pk_fp8_f32 v56, v45, v44 op_sel:[0,0,1]
	v_ashrrev_i32_e32 v49, 31, v48
	v_lshlrev_b64 v[44:45], 6, v[48:49]
	v_lshl_add_u64 v[44:45], v[92:93], 0, v[44:45]
	global_store_dword v[44:45], v56, off
	ds_read_b128 v[52:55], v50 offset:64
	v_mov_b32_e32 v56, v89
	s_waitcnt lgkmcnt(0)
	v_add_f32_e32 v40, v40, v52
	v_add_f32_e32 v41, v41, v53
	v_max_f32_e32 v52, 0, v40
	v_max_f32_e32 v53, 0, v41
	v_mul_f32_e32 v40, 0x42800000, v52
	v_mul_f32_e32 v41, 0x42800000, v53
	v_min_f32_e32 v40, 0x43e00000, v40
	v_min_f32_e32 v41, 0x43e00000, v41
	v_add_f32_e32 v42, v42, v54
	v_add_f32_e32 v43, v43, v55
	v_cvt_pk_fp8_f32 v56, v40, v41
	v_max_f32_e32 v54, 0, v42
	v_max_f32_e32 v55, 0, v43
	v_mul_f32_e32 v42, 0x42800000, v54
	v_mul_f32_e32 v40, 0x42800000, v55
	v_min_f32_e32 v41, 0x43e00000, v42
	v_min_f32_e32 v40, 0x43e00000, v40
	v_cvt_pk_fp8_f32 v56, v41, v40 op_sel:[0,0,1]
	global_store_dword v[44:45], v56, off offset:16
	ds_read_b128 v[40:43], v50 offset:128
	v_mov_b32_e32 v56, v89
	s_waitcnt lgkmcnt(0)
	v_add_f32_e32 v36, v36, v40
	v_add_f32_e32 v37, v37, v41
	v_max_f32_e32 v59, 0, v36
	v_max_f32_e32 v60, 0, v37
	v_mul_f32_e32 v36, 0x42800000, v59
	v_mul_f32_e32 v37, 0x42800000, v60
	v_min_f32_e32 v36, 0x43e00000, v36
	v_min_f32_e32 v37, 0x43e00000, v37
	v_add_f32_e32 v38, v38, v42
	v_add_f32_e32 v39, v39, v43
	v_cvt_pk_fp8_f32 v56, v36, v37
	v_max_f32_e32 v61, 0, v38
	v_max_f32_e32 v62, 0, v39
	v_mul_f32_e32 v38, 0x42800000, v61
	v_mul_f32_e32 v36, 0x42800000, v62
	v_min_f32_e32 v37, 0x43e00000, v38
	v_min_f32_e32 v36, 0x43e00000, v36
	v_cvt_pk_fp8_f32 v56, v37, v36 op_sel:[0,0,1]
	v_lshlrev_b64 v[40:41], 7, v[48:49]
	v_lshl_add_u64 v[40:41], v[90:91], 0, v[40:41]
	v_cvt_pk_f16_f32 v43, v46, v47
	global_store_dword v[44:45], v56, off offset:32
	ds_read_b128 v[36:39], v50 offset:192
	v_cvt_pk_f16_f32 v42, v57, v58
	global_store_dwordx2 v[40:41], v[42:43], off
	v_cvt_pk_f16_f32 v43, v54, v55
	v_cvt_pk_f16_f32 v42, v52, v53
	global_store_dwordx2 v[40:41], v[42:43], off offset:32
	v_cvt_pk_f16_f32 v43, v61, v62
	v_cvt_pk_f16_f32 v42, v59, v60
	global_store_dwordx2 v[40:41], v[42:43], off offset:64
	s_waitcnt lgkmcnt(0)
	v_add_f32_e32 v32, v32, v36
	v_add_f32_e32 v33, v33, v37
	v_add_f32_e32 v34, v34, v38
	v_add_f32_e32 v35, v35, v39
	v_max_f32_e32 v32, 0, v32
	v_max_f32_e32 v36, 0, v33
	v_max_f32_e32 v33, 0, v34
	v_max_f32_e32 v34, 0, v35
	v_mul_f32_e32 v35, 0x42800000, v32
	v_mul_f32_e32 v37, 0x42800000, v36
	v_min_f32_e32 v35, 0x43e00000, v35
	v_min_f32_e32 v37, 0x43e00000, v37
	v_mov_b32_e32 v39, v89
	v_cvt_pk_fp8_f32 v39, v35, v37
	v_mul_f32_e32 v38, 0x42800000, v33
	v_mul_f32_e32 v37, 0x42800000, v34
	v_min_f32_e32 v35, 0x43e00000, v38
	v_min_f32_e32 v37, 0x43e00000, v37
	v_cvt_pk_fp8_f32 v39, v35, v37 op_sel:[0,0,1]
	v_cvt_pk_f16_f32 v33, v33, v34
	v_cvt_pk_f16_f32 v32, v32, v36
	global_store_dwordx2 v[40:41], v[32:33], off offset:96
	global_store_dword v[44:45], v39, off offset:48
	s_branch .LBB4_15

	.amdhsa_kernel _Z7k_layerILi1EEvPKDF16_PKiPKjS3_S3_S1_PKfPDF16_PhS3_S7_Pf
		.amdhsa_group_segment_fixed_size 256
		.amdhsa_private_segment_fixed_size 0
		.amdhsa_kernarg_size 352
		.amdhsa_user_sgpr_count 2
		.amdhsa_user_sgpr_dispatch_ptr 0
		.amdhsa_user_sgpr_queue_ptr 0
		.amdhsa_user_sgpr_kernarg_segment_ptr 1
		.amdhsa_user_sgpr_dispatch_id 0
		.amdhsa_user_sgpr_kernarg_preload_length 0
		.amdhsa_user_sgpr_kernarg_preload_offset 0
		.amdhsa_user_sgpr_private_segment_size 0
		.amdhsa_uses_dynamic_stack 0
		.amdhsa_enable_private_segment 0
		.amdhsa_system_sgpr_workgroup_id_x 1
		.amdhsa_system_sgpr_workgroup_id_y 0
		.amdhsa_system_sgpr_workgroup_id_z 0
		.amdhsa_system_sgpr_workgroup_info 0
		.amdhsa_system_vgpr_workitem_id 0
		.amdhsa_next_free_vgpr 114
		.amdhsa_next_free_sgpr 32
		.amdhsa_accum_offset 116
		.amdhsa_reserve_vcc 1
		.amdhsa_float_round_mode_32 0
		.amdhsa_float_round_mode_16_64 0
		.amdhsa_float_denorm_mode_32 3
		.amdhsa_float_denorm_mode_16_64 3
		.amdhsa_dx10_clamp 1
		.amdhsa_ieee_mode 1
		.amdhsa_fp16_overflow 0
		.amdhsa_tg_split 0
		.amdhsa_exception_fp_ieee_invalid_op 0
		.amdhsa_exception_fp_denorm_src 0
		.amdhsa_exception_fp_ieee_div_zero 0
		.amdhsa_exception_fp_ieee_overflow 0
		.amdhsa_exception_fp_ieee_underflow 0
		.amdhsa_exception_fp_ieee_inexact 0
		.amdhsa_exception_int_div_zero 0
	.end_amdhsa_kernel

_Z7k_layerILi2EEvPKDF16_PKiPKjS3_S3_S1_PKfPDF16_PhS3_S7_Pf:
	s_load_dwordx2 s[24:25], s[0:1], 0x58
	s_load_dwordx4 s[12:15], s[0:1], 0x0
	s_load_dwordx2 s[26:27], s[0:1], 0x10
	s_load_dwordx4 s[16:19], s[0:1], 0x48
	s_load_dwordx4 s[20:23], s[0:1], 0x28
	v_lshrrev_b32_e32 v2, 5, v0
	v_and_b32_e32 v4, 31, v0
	v_mul_u32_u24_e32 v3, 0x210, v2
	v_lshlrev_b32_e32 v5, 4, v4
	v_add3_u32 v4, v3, v5, 0
	v_lshl_or_b32 v2, v2, 9, v5
	v_mov_b32_e32 v3, 0
	v_or_b32_e32 v1, 0xfffffc00, v0
	s_waitcnt lgkmcnt(0)
	v_add_u32_e32 v3, 0x4000, v2
	v_lshlrev_b32_e32 v14, 4, v0
	v_add_u32_e32 v15, 0xffffff00, v14
	s_mov_b64 s[4:5], exec
	v_cmp_gt_u32_e32 vcc, 16, v0
	v_cmp_gt_u32_e64 s[6:7], 48, v0
	s_andn2_b64 s[8:9], s[6:7], vcc
	s_and_b64 exec, s[4:5], vcc
	global_load_dwordx4 v[16:19], v14, s[22:23]
	s_and_b64 exec, s[4:5], s[8:9]
	global_load_dwordx4 v[16:19], v15, s[18:19]
	s_mov_b64 exec, s[4:5]
	global_load_dwordx4 v[6:9], v2, s[20:21]
	global_load_dwordx4 v[10:13], v3, s[20:21]
	s_waitcnt vmcnt(1)
	ds_write_b128 v4, v[6:9]
	s_waitcnt vmcnt(0)
	ds_write_b128 v4, v[10:13] offset:16896
	s_and_b64 exec, s[4:5], s[6:7]
	ds_write_b128 v14, v[16:19] offset:52240
	s_mov_b64 exec, s[4:5]
	s_mov_b32 s4, 0
	v_cmp_eq_u32_e32 vcc, 0, v0
	s_and_saveexec_b64 s[6:7], vcc
	v_mov_b32_e32 v1, 0
	ds_write_b32 v1, v1 offset:52224
	s_or_b64 exec, exec, s[6:7]
	s_waitcnt lgkmcnt(0)
	s_barrier
	s_load_dword s8, s[0:1], 0x60
	s_mul_hi_u32 s5, s2, 0x186a0
	s_cmp_lg_u64 s[4:5], 0
	s_mul_i32 s3, s2, 0x186a0
	s_waitcnt lgkmcnt(0)
	v_cvt_f32_u32_e32 v1, s8
	s_cbranch_scc0 .LBB5_119
	v_fmamk_f32 v2, 0, 0x4f800000, v1
	v_rcp_f32_e32 v2, v2
	s_sub_u32 s4, 0, s8
	s_subb_u32 s9, 0, 0
	v_mul_f32_e32 v2, 0x5f7ffffc, v2
	v_mul_f32_e32 v3, 0x2f800000, v2
	v_trunc_f32_e32 v3, v3
	v_fmamk_f32 v2, v3, 0xcf800000, v2
	v_cvt_u32_f32_e32 v3, v3
	v_cvt_u32_f32_e32 v2, v2
	v_readfirstlane_b32 s20, v3
	v_readfirstlane_b32 s10, v2
	s_mul_hi_u32 s21, s4, s10
	s_mul_i32 s28, s4, s20
	s_mul_i32 s11, s9, s10
	s_add_i32 s21, s21, s28
	s_add_i32 s21, s21, s11
	s_mul_i32 s29, s4, s10
	s_mul_i32 s28, s10, s21
	s_mul_hi_u32 s30, s10, s29
	s_mul_hi_u32 s11, s10, s21
	s_add_u32 s28, s30, s28
	s_addc_u32 s11, 0, s11
	s_mul_hi_u32 s31, s20, s29
	s_mul_i32 s29, s20, s29
	s_add_u32 s28, s28, s29
	s_mul_hi_u32 s30, s20, s21
	s_addc_u32 s11, s11, s31
	s_addc_u32 s28, s30, 0
	s_mul_i32 s21, s20, s21
	s_add_u32 s11, s11, s21
	s_addc_u32 s21, 0, s28
	s_add_u32 s28, s10, s11
	s_cselect_b64 s[10:11], -1, 0
	s_cmp_lg_u64 s[10:11], 0
	s_addc_u32 s20, s20, s21
	s_mul_i32 s10, s4, s20
	s_mul_hi_u32 s11, s4, s28
	s_add_i32 s10, s11, s10
	s_mul_i32 s9, s9, s28
	s_add_i32 s10, s10, s9
	s_mul_i32 s4, s4, s28
	s_mul_hi_u32 s11, s20, s4
	s_mul_i32 s21, s20, s4
	s_mul_i32 s30, s28, s10
	s_mul_hi_u32 s4, s28, s4
	s_mul_hi_u32 s29, s28, s10
	s_add_u32 s4, s4, s30
	s_addc_u32 s29, 0, s29
	s_add_u32 s4, s4, s21
	s_mul_hi_u32 s9, s20, s10
	s_addc_u32 s4, s29, s11
	s_addc_u32 s9, s9, 0
	s_mul_i32 s10, s20, s10
	s_add_u32 s4, s4, s10
	s_addc_u32 s9, 0, s9
	s_add_u32 s4, s28, s4
	s_cselect_b64 s[10:11], -1, 0
	s_cmp_lg_u64 s[10:11], 0
	s_addc_u32 s9, s20, s9
	s_mul_i32 s11, s3, s9
	s_mul_hi_u32 s20, s3, s4
	s_mul_hi_u32 s10, s3, s9
	s_add_u32 s11, s20, s11
	s_addc_u32 s10, 0, s10
	s_mul_hi_u32 s21, s5, s4
	s_mul_i32 s4, s5, s4
	s_add_u32 s4, s11, s4
	s_mul_hi_u32 s20, s5, s9
	s_addc_u32 s4, s10, s21
	s_addc_u32 s10, s20, 0
	s_mul_i32 s9, s5, s9
	s_add_u32 s9, s4, s9
	s_addc_u32 s4, 0, s10
	s_mul_i32 s4, s8, s4
	s_mul_hi_u32 s10, s8, s9
	s_add_u32 s20, s9, 1
	s_add_u32 s21, s9, 2
	s_add_i32 s4, s10, s4
	s_mul_i32 s10, s8, s9
	s_sub_u32 s28, s3, s10
	s_cselect_b64 s[10:11], -1, 0
	s_cmp_lg_u64 s[10:11], 0
	s_subb_u32 s10, s5, s4
	s_sub_u32 s11, s28, s8
	s_cselect_b64 s[4:5], -1, 0
	s_cmp_lg_u64 s[4:5], 0
	s_subb_u32 s4, s10, 0
	s_cmp_ge_u32 s11, s8
	s_cselect_b32 s5, -1, 0
	s_cmp_eq_u32 s4, 0
	s_cselect_b32 s4, s5, -1
	s_cmp_lg_u32 s4, 0
	s_cselect_b32 s4, s21, s20
	s_cmp_ge_u32 s28, s8
	s_cselect_b32 s5, -1, 0
	s_cmp_eq_u32 s10, 0
	s_cselect_b32 s5, s5, -1
	s_cmp_lg_u32 s5, 0
	s_cselect_b32 s20, s4, s9
	v_cvt_f32_u32_e32 v2, s8
	s_cbranch_execnz .LBB5_7

.LBB5_105:
	s_cbranch_execz .LBB5_102
	ds_write_b128 v82, v[4:7] offset:33792
	ds_read_b128 v[4:7], v83 offset:256
	ds_read_b128 v[24:27], v80 offset:33792
	ds_read_b128 v[28:31], v83 offset:8704
	s_waitcnt lgkmcnt(1)
	v_mfma_f32_16x16x32_f16 v[4:7], v[4:7], v[24:27], v[8:11]
	s_nop 2
	ds_read_b128 v[8:11], v83 offset:17152
	s_waitcnt lgkmcnt(1)
	v_mfma_f32_16x16x32_f16 v[12:15], v[28:31], v[24:27], v[12:15]
	s_waitcnt lgkmcnt(0)
	v_mfma_f32_16x16x32_f16 v[8:11], v[8:11], v[24:27], v[16:19]
	s_nop 2
	ds_read_b128 v[16:19], v83 offset:25600
	s_waitcnt lgkmcnt(0)
	v_mfma_f32_16x16x32_f16 v[16:19], v[16:19], v[24:27], v[20:23]
	s_nop 2
	ds_read_b128 v[20:23], v83 offset:320
	ds_read_b128 v[24:27], v80 offset:33856
	ds_read_b128 v[28:31], v83 offset:8768
	s_waitcnt lgkmcnt(1)
	v_mfma_f32_16x16x32_f16 v[4:7], v[20:23], v[24:27], v[4:7]
	ds_read_b128 v[20:23], v83 offset:17216
	s_waitcnt lgkmcnt(1)
	v_mfma_f32_16x16x32_f16 v[12:15], v[28:31], v[24:27], v[12:15]
	s_waitcnt lgkmcnt(0)
	v_mfma_f32_16x16x32_f16 v[8:11], v[20:23], v[24:27], v[8:11]
	ds_read_b128 v[20:23], v83 offset:25664
	ds_write_b128 v82, v[0:3] offset:33792
	s_waitcnt lgkmcnt(1)
	v_mfma_f32_16x16x32_f16 v[0:3], v[20:23], v[24:27], v[16:19]
	s_nop 2
	ds_read_b128 v[16:19], v83 offset:384
	ds_read_b128 v[20:23], v80 offset:33792
	ds_read_b128 v[24:27], v83 offset:8832
	s_waitcnt lgkmcnt(1)
	v_mfma_f32_16x16x32_f16 v[4:7], v[16:19], v[20:23], v[4:7]
	ds_read_b128 v[16:19], v83 offset:17280
	s_waitcnt lgkmcnt(1)
	v_mfma_f32_16x16x32_f16 v[12:15], v[24:27], v[20:23], v[12:15]
	s_waitcnt lgkmcnt(0)
	v_mfma_f32_16x16x32_f16 v[8:11], v[16:19], v[20:23], v[8:11]
	ds_read_b128 v[16:19], v83 offset:25728
	s_waitcnt lgkmcnt(0)
	v_mfma_f32_16x16x32_f16 v[0:3], v[16:19], v[20:23], v[0:3]
	ds_read_b128 v[16:19], v83 offset:448
	ds_read_b128 v[20:23], v80 offset:33856
	ds_read_b128 v[24:27], v83 offset:8896
	ds_read_b128 v[28:31], v83 offset:17344
	ds_read_b128 v[50:53], v83 offset:25792
	s_mov_b64 s[6:7], s[22:23]
	s_mov_b64 s[8:9], s[18:19]
	s_waitcnt lgkmcnt(1)
	v_mfma_f32_16x16x32_f16 v[8:11], v[28:31], v[20:23], v[8:11]
	s_nop 0
	s_waitcnt lgkmcnt(0)
	v_mfma_f32_16x16x32_f16 v[0:3], v[50:53], v[20:23], v[0:3]
	v_mfma_f32_16x16x32_f16 v[16:19], v[16:19], v[20:23], v[4:7]
	s_nop 2
	v_add_u32_e32 v6, s33, v77
	v_mfma_f32_16x16x32_f16 v[12:15], v[24:27], v[20:23], v[12:15]
	v_cmp_gt_i32_e32 vcc, s28, v6
	ds_read_b128 v[20:23], v32 offset:52240
	ds_read_b128 v[24:27], v32 offset:52496
	ds_read_b128 v[28:31], v32 offset:52752
	s_waitcnt lgkmcnt(0)
	v_add_f32_e32 v7, v16, v20
	v_mov_b32_e32 v4, v24
	v_mov_b32_e32 v5, v28
	v_add_f32_e32 v16, v17, v21
	v_add_f32_e32 v17, v18, v22
	v_add_f32_e32 v18, v19, v23
	v_max_f32_e32 v24, 0, v7
	v_max_f32_e32 v62, 0, v16
	v_max_f32_e32 v64, 0, v17
	v_max_f32_e32 v66, 0, v18
	ds_read_b128 v[16:19], v32 offset:52304
	ds_read_b128 v[20:23], v32 offset:52560
	ds_read_b128 v[50:53], v32 offset:52816
	s_waitcnt lgkmcnt(0)
	v_add_f32_e32 v7, v12, v16
	v_add_f32_e32 v12, v13, v17
	v_add_f32_e32 v13, v14, v18
	v_add_f32_e32 v14, v15, v19
	v_max_f32_e32 v68, 0, v7
	v_max_f32_e32 v70, 0, v12
	v_max_f32_e32 v72, 0, v13
	v_max_f32_e32 v86, 0, v14
	ds_read_b128 v[12:15], v32 offset:52368
	ds_read_b128 v[16:19], v32 offset:52624
	ds_read_b128 v[54:57], v32 offset:52880
	v_pk_fma_f32 v[88:89], v[4:5], v[24:25], 0 op_sel_hi:[1,0,0]
	v_mov_b32_e32 v28, v25
	v_mov_b32_e32 v24, v26
	v_mov_b32_e32 v25, v30
	v_mov_b32_e32 v30, v27
	v_mov_b32_e32 v26, v20
	v_mov_b32_e32 v27, v50
	v_mov_b32_e32 v50, v21
	v_mov_b32_e32 v20, v22
	v_mov_b32_e32 v21, v52
	v_mov_b32_e32 v52, v23
	v_pk_fma_f32 v[22:23], v[28:29], v[62:63], v[88:89] op_sel_hi:[1,0,1]
	v_mov_b32_e32 v4, v33
	v_pk_fma_f32 v[22:23], v[24:25], v[64:65], v[22:23] op_sel_hi:[1,0,1]
	v_mov_b32_e32 v5, v33
	v_pk_fma_f32 v[22:23], v[30:31], v[66:67], v[22:23] op_sel_hi:[1,0,1]
	s_waitcnt lgkmcnt(0)
	v_add_f32_e32 v7, v8, v12
	v_pk_fma_f32 v[22:23], v[26:27], v[68:69], v[22:23] op_sel_hi:[1,0,1]
	v_mov_b32_e32 v8, v16
	v_pk_fma_f32 v[22:23], v[50:51], v[70:71], v[22:23] op_sel_hi:[1,0,1]
	v_add_f32_e32 v11, v11, v15
	v_pk_fma_f32 v[20:21], v[20:21], v[72:73], v[22:23] op_sel_hi:[1,0,1]
	v_add_f32_e32 v22, v9, v13
	v_pk_fma_f32 v[20:21], v[52:53], v[86:87], v[20:21] op_sel_hi:[1,0,1]
	v_add_f32_e32 v23, v10, v14
	v_mov_b32_e32 v9, v54
	v_max_f32_e32 v10, 0, v7
	v_mov_b32_e32 v54, v17
	v_max_f32_e32 v14, 0, v22
	v_pk_fma_f32 v[8:9], v[8:9], v[10:11], v[20:21] op_sel_hi:[1,0,1]
	v_mov_b32_e32 v12, v18
	v_mov_b32_e32 v13, v56
	v_max_f32_e32 v16, 0, v23
	v_pk_fma_f32 v[8:9], v[54:55], v[14:15], v[8:9] op_sel_hi:[1,0,1]
	v_max_f32_e32 v22, 0, v11
	v_pk_fma_f32 v[8:9], v[12:13], v[16:17], v[8:9] op_sel_hi:[1,0,1]
	v_mov_b32_e32 v56, v19
	ds_read_b128 v[10:13], v32 offset:52432
	ds_read_b128 v[14:17], v32 offset:52688
	ds_read_b128 v[18:21], v32 offset:52944
	v_pk_fma_f32 v[22:23], v[56:57], v[22:23], v[8:9] op_sel_hi:[1,0,1]
	v_and_b32_e32 v24, 64, v84
	v_xor_b32_e32 v7, 16, v84
	v_add_u32_e32 v8, 64, v24
	v_cmp_lt_i32_e64 s[6:7], v7, v8
	s_and_b64 s[8:9], s[2:3], vcc
	s_waitcnt lgkmcnt(0)
	v_add_f32_e32 v9, v0, v10
	v_add_f32_e32 v11, v1, v11
	v_mov_b32_e32 v0, v14
	v_mov_b32_e32 v1, v18
	v_max_f32_e32 v10, 0, v9
	v_add_f32_e32 v24, v2, v12
	v_add_f32_e32 v13, v3, v13
	v_mov_b32_e32 v18, v15
	v_max_f32_e32 v12, 0, v11
	v_pk_fma_f32 v[0:1], v[0:1], v[10:11], v[22:23] op_sel_hi:[1,0,1]
	v_mov_b32_e32 v2, v16
	v_mov_b32_e32 v3, v20
	v_max_f32_e32 v14, 0, v24
	v_pk_fma_f32 v[0:1], v[18:19], v[12:13], v[0:1] op_sel_hi:[1,0,1]
	v_cndmask_b32_e64 v7, v84, v7, s[6:7]
	v_mov_b32_e32 v20, v17
	v_max_f32_e32 v16, 0, v13
	v_pk_fma_f32 v[0:1], v[2:3], v[14:15], v[0:1] op_sel_hi:[1,0,1]
	v_lshlrev_b32_e32 v7, 2, v7
	v_pk_fma_f32 v[0:1], v[20:21], v[16:17], v[0:1] op_sel_hi:[1,0,1]
	ds_bpermute_b32 v2, v7, v0
	ds_bpermute_b32 v3, v7, v1
	v_xor_b32_e32 v7, 32, v84
	v_cmp_lt_i32_e64 s[6:7], v7, v8
	v_mov_b32_e32 v10, -1
	s_waitcnt lgkmcnt(0)
	v_pk_add_f32 v[0:1], v[0:1], v[2:3]
	v_cndmask_b32_e64 v7, v84, v7, s[6:7]
	v_lshlrev_b32_e32 v7, 2, v7
	ds_bpermute_b32 v2, v7, v0
	ds_bpermute_b32 v3, v7, v1
	v_mov_b32_e32 v7, 0
	s_and_saveexec_b64 s[6:7], s[8:9]
	s_cbranch_execz .LBB5_108
	v_ashrrev_i32_e32 v7, 31, v6
	v_lshl_add_u64 v[4:5], v[6:7], 2, s[16:17]
	global_load_dword v10, v[4:5], off
	s_waitcnt lgkmcnt(0)
	v_pk_add_f32 v[4:5], v[0:1], v[2:3]
	v_mov_b32_e32 v7, 1.0

	.amdhsa_kernel _Z7k_layerILi2EEvPKDF16_PKiPKjS3_S3_S1_PKfPDF16_PhS3_S7_Pf
		.amdhsa_group_segment_fixed_size 768
		.amdhsa_private_segment_fixed_size 0
		.amdhsa_kernarg_size 352
		.amdhsa_user_sgpr_count 2
		.amdhsa_user_sgpr_dispatch_ptr 0
		.amdhsa_user_sgpr_queue_ptr 0
		.amdhsa_user_sgpr_kernarg_segment_ptr 1
		.amdhsa_user_sgpr_dispatch_id 0
		.amdhsa_user_sgpr_kernarg_preload_length 0
		.amdhsa_user_sgpr_kernarg_preload_offset 0
		.amdhsa_user_sgpr_private_segment_size 0
		.amdhsa_uses_dynamic_stack 0
		.amdhsa_enable_private_segment 0
		.amdhsa_system_sgpr_workgroup_id_x 1
		.amdhsa_system_sgpr_workgroup_id_y 0
		.amdhsa_system_sgpr_workgroup_id_z 0
		.amdhsa_system_sgpr_workgroup_info 0
		.amdhsa_system_vgpr_workitem_id 0
		.amdhsa_next_free_vgpr 102
		.amdhsa_next_free_sgpr 38
		.amdhsa_accum_offset 104
		.amdhsa_reserve_vcc 1
		.amdhsa_float_round_mode_32 0
		.amdhsa_float_round_mode_16_64 0
		.amdhsa_float_denorm_mode_32 3
		.amdhsa_float_denorm_mode_16_64 3
		.amdhsa_dx10_clamp 1
		.amdhsa_ieee_mode 1
		.amdhsa_fp16_overflow 0
		.amdhsa_tg_split 0
		.amdhsa_exception_fp_ieee_invalid_op 0
		.amdhsa_exception_fp_denorm_src 0
		.amdhsa_exception_fp_ieee_div_zero 0
		.amdhsa_exception_fp_ieee_overflow 0
		.amdhsa_exception_fp_ieee_underflow 0
		.amdhsa_exception_fp_ieee_inexact 0
		.amdhsa_exception_int_div_zero 0
	.end_amdhsa_kernel

amdhsa.kernels:
  - .agpr_count:     0
    .args:
      - .actual_access:  read_only
        .address_space:  global
        .offset:         0
        .size:           8
        .value_kind:     global_buffer
      - .actual_access:  read_only
        .address_space:  global
        .offset:         8
        .size:           8
        .value_kind:     global_buffer
      - .actual_access:  read_only
        .address_space:  global
        .offset:         16
        .size:           8
        .value_kind:     global_buffer
      - .actual_access:  read_only
        .address_space:  global
        .offset:         24
        .size:           8
        .value_kind:     global_buffer
      - .actual_access:  read_only
        .address_space:  global
        .offset:         32
        .size:           8
        .value_kind:     global_buffer
      - .actual_access:  read_only
        .address_space:  global
        .offset:         40
        .size:           8
        .value_kind:     global_buffer
      - .actual_access:  read_only
        .address_space:  global
        .offset:         48
        .size:           8
        .value_kind:     global_buffer
      - .actual_access:  read_only
        .address_space:  global
        .offset:         56
        .size:           8
        .value_kind:     global_buffer
      - .actual_access:  read_only
        .address_space:  global
        .offset:         64
        .size:           8
        .value_kind:     global_buffer
      - .actual_access:  read_only
        .address_space:  global
        .offset:         72
        .size:           8
        .value_kind:     global_buffer
      - .actual_access:  read_only
        .address_space:  global
        .offset:         80
        .size:           8
        .value_kind:     global_buffer
      - .actual_access:  read_only
        .address_space:  global
        .offset:         88
        .size:           8
        .value_kind:     global_buffer
      - .actual_access:  write_only
        .address_space:  global
        .offset:         96
        .size:           8
        .value_kind:     global_buffer
      - .actual_access:  write_only
        .address_space:  global
        .offset:         104
        .size:           8
        .value_kind:     global_buffer
      - .actual_access:  write_only
        .address_space:  global
        .offset:         112
        .size:           8
        .value_kind:     global_buffer
      - .actual_access:  write_only
        .address_space:  global
        .offset:         120
        .size:           8
        .value_kind:     global_buffer
      - .actual_access:  write_only
        .address_space:  global
        .offset:         128
        .size:           8
        .value_kind:     global_buffer
      - .actual_access:  write_only
        .address_space:  global
        .offset:         136
        .size:           8
        .value_kind:     global_buffer
      - .actual_access:  write_only
        .address_space:  global
        .offset:         144
        .size:           8
        .value_kind:     global_buffer
      - .actual_access:  write_only
        .address_space:  global
        .offset:         152
        .size:           8
        .value_kind:     global_buffer
      - .actual_access:  write_only
        .address_space:  global
        .offset:         160
        .size:           8
        .value_kind:     global_buffer
    .group_segment_fixed_size: 0
    .kernarg_segment_align: 8
    .kernarg_segment_size: 168
    .language:       OpenCL C
    .language_version:
      - 2
      - 0
    .max_flat_workgroup_size: 1024
    .name:           _Z6k_prepPKiS0_PKfS2_S2_S2_S2_S2_S2_S2_S2_S2_PDF16_S3_S3_PfS4_S4_PjS3_S5_
    .private_segment_fixed_size: 0
    .sgpr_count:     27
    .sgpr_spill_count: 0
    .symbol:         _Z6k_prepPKiS0_PKfS2_S2_S2_S2_S2_S2_S2_S2_S2_PDF16_S3_S3_PfS4_S4_PjS3_S5_.kd
    .uniform_work_group_size: 1
    .uses_dynamic_stack: false
    .vgpr_count:     61
    .vgpr_spill_count: 0
    .wavefront_size: 64
  - .agpr_count:     0
    .args:
      - .actual_access:  read_only
        .address_space:  global
        .offset:         0
        .size:           8
        .value_kind:     global_buffer
      - .actual_access:  read_only
        .address_space:  global
        .offset:         8
        .size:           8
        .value_kind:     global_buffer
      - .actual_access:  read_only
        .address_space:  global
        .offset:         16
        .size:           8
        .value_kind:     global_buffer
      - .actual_access:  write_only
        .address_space:  global
        .offset:         24
        .size:           8
        .value_kind:     global_buffer
      - .actual_access:  write_only
        .address_space:  global
        .offset:         32
        .size:           8
        .value_kind:     global_buffer
      - .actual_access:  write_only
        .address_space:  global
        .offset:         40
        .size:           8
        .value_kind:     global_buffer
      - .actual_access:  read_only
        .address_space:  global
        .offset:         48
        .size:           8
        .value_kind:     global_buffer
      - .actual_access:  read_only
        .address_space:  global
        .offset:         56
        .size:           8
        .value_kind:     global_buffer
      - .actual_access:  read_only
        .address_space:  global
        .offset:         64
        .size:           8
        .value_kind:     global_buffer
      - .actual_access:  read_only
        .address_space:  global
        .offset:         72
        .size:           8
        .value_kind:     global_buffer
      - .actual_access:  read_only
        .address_space:  global
        .offset:         80
        .size:           8
        .value_kind:     global_buffer
      - .actual_access:  read_only
        .address_space:  global
        .offset:         88
        .size:           8
        .value_kind:     global_buffer
      - .actual_access:  read_only
        .address_space:  global
        .offset:         96
        .size:           8
        .value_kind:     global_buffer
      - .actual_access:  read_only
        .address_space:  global
        .offset:         104
        .size:           8
        .value_kind:     global_buffer
      - .actual_access:  read_only
        .address_space:  global
        .offset:         112
        .size:           8
        .value_kind:     global_buffer
      - .actual_access:  read_only
        .address_space:  global
        .offset:         120
        .size:           8
        .value_kind:     global_buffer
      - .actual_access:  read_only
        .address_space:  global
        .offset:         128
        .size:           8
        .value_kind:     global_buffer
      - .actual_access:  write_only
        .address_space:  global
        .offset:         136
        .size:           8
        .value_kind:     global_buffer
      - .actual_access:  write_only
        .address_space:  global
        .offset:         144
        .size:           8
        .value_kind:     global_buffer
      - .actual_access:  write_only
        .address_space:  global
        .offset:         152
        .size:           8
        .value_kind:     global_buffer
      - .actual_access:  write_only
        .address_space:  global
        .offset:         160
        .size:           8
        .value_kind:     global_buffer
      - .actual_access:  write_only
        .address_space:  global
        .offset:         168
        .size:           8
        .value_kind:     global_buffer
    .group_segment_fixed_size: 1696
    .kernarg_segment_align: 8
    .kernarg_segment_size: 176
    .language:       OpenCL C
    .language_version:
      - 2
      - 0
    .max_flat_workgroup_size: 1024
    .name:           _Z11k_localsortPKiS0_S0_PjPtPiPKjPKfS7_S7_S7_S7_S7_S7_S7_S7_S7_PDF16_S8_S8_PfS9_
    .private_segment_fixed_size: 0
    .sgpr_count:     71
    .sgpr_spill_count: 0
    .symbol:         _Z11k_localsortPKiS0_S0_PjPtPiPKjPKfS7_S7_S7_S7_S7_S7_S7_S7_S7_PDF16_S8_S8_PfS9_.kd
    .uniform_work_group_size: 1
    .uses_dynamic_stack: false
    .vgpr_count:     95
    .vgpr_spill_count: 0
    .wavefront_size: 64
  - .agpr_count:     0
    .args:
      - .actual_access:  read_only
        .address_space:  global
        .offset:         0
        .size:           8
        .value_kind:     global_buffer
      - .actual_access:  read_only
        .address_space:  global
        .offset:         8
        .size:           8
        .value_kind:     global_buffer
      - .actual_access:  read_only
        .address_space:  global
        .offset:         16
        .size:           8
        .value_kind:     global_buffer
      - .actual_access:  write_only
        .address_space:  global
        .offset:         24
        .size:           8
        .value_kind:     global_buffer
      - .actual_access:  write_only
        .address_space:  global
        .offset:         32
        .size:           8
        .value_kind:     global_buffer
    .group_segment_fixed_size: 54144
    .kernarg_segment_align: 8
    .kernarg_segment_size: 40
    .language:       OpenCL C
    .language_version:
      - 2
      - 0
    .max_flat_workgroup_size: 1024
    .name:           _Z12k_bucketsortPKjPKtPKiPiPj
    .private_segment_fixed_size: 0
    .sgpr_count:     70
    .sgpr_spill_count: 0
    .symbol:         _Z12k_bucketsortPKjPKtPKiPiPj.kd
    .uniform_work_group_size: 1
    .uses_dynamic_stack: false
    .vgpr_count:     59
    .vgpr_spill_count: 0
    .wavefront_size: 64
  - .agpr_count:     0
    .args:
      - .actual_access:  read_only
        .address_space:  global
        .offset:         0
        .size:           8
        .value_kind:     global_buffer
      - .actual_access:  read_only
        .address_space:  global
        .offset:         8
        .size:           8
        .value_kind:     global_buffer
      - .actual_access:  write_only
        .address_space:  global
        .offset:         16
        .size:           8
        .value_kind:     global_buffer
    .group_segment_fixed_size: 0
    .kernarg_segment_align: 8
    .kernarg_segment_size: 24
    .language:       OpenCL C
    .language_version:
      - 2
      - 0
    .max_flat_workgroup_size: 256
    .name:           _Z7k_finalPKfS0_Pf
    .private_segment_fixed_size: 0
    .sgpr_count:     14
    .sgpr_spill_count: 0
    .symbol:         _Z7k_finalPKfS0_Pf.kd
    .uniform_work_group_size: 1
    .uses_dynamic_stack: false
    .vgpr_count:     10
    .vgpr_spill_count: 0
    .wavefront_size: 64
  - .agpr_count:     0
    .args:
      - .actual_access:  read_only
        .address_space:  global
        .offset:         0
        .size:           8
        .value_kind:     global_buffer
      - .actual_access:  read_only
        .address_space:  global
        .offset:         8
        .size:           8
        .value_kind:     global_buffer
      - .actual_access:  read_only
        .address_space:  global
        .offset:         16
        .size:           8
        .value_kind:     global_buffer
      - .actual_access:  read_only
        .address_space:  global
        .offset:         24
        .size:           8
        .value_kind:     global_buffer
      - .actual_access:  read_only
        .address_space:  global
        .offset:         32
        .size:           8
        .value_kind:     global_buffer
      - .actual_access:  read_only
        .address_space:  global
        .offset:         40
        .size:           8
        .value_kind:     global_buffer
      - .address_space:  global
        .offset:         48
        .size:           8
        .value_kind:     global_buffer
      - .actual_access:  write_only
        .address_space:  global
        .offset:         56
        .size:           8
        .value_kind:     global_buffer
      - .address_space:  global
        .offset:         64
        .size:           8
        .value_kind:     global_buffer
      - .actual_access:  read_only
        .address_space:  global
        .offset:         72
        .size:           8
        .value_kind:     global_buffer
      - .address_space:  global
        .offset:         80
        .size:           8
        .value_kind:     global_buffer
      - .actual_access:  read_only
        .address_space:  global
        .offset:         88
        .size:           8
        .value_kind:     global_buffer
      - .offset:         96
        .size:           4
        .value_kind:     hidden_block_count_x
      - .offset:         100
        .size:           4
        .value_kind:     hidden_block_count_y
      - .offset:         104
        .size:           4
        .value_kind:     hidden_block_count_z
      - .offset:         108
        .size:           2
        .value_kind:     hidden_group_size_x
      - .offset:         110
        .size:           2
        .value_kind:     hidden_group_size_y
      - .offset:         112
        .size:           2
        .value_kind:     hidden_group_size_z
      - .offset:         114
        .size:           2
        .value_kind:     hidden_remainder_x
      - .offset:         116
        .size:           2
        .value_kind:     hidden_remainder_y
      - .offset:         118
        .size:           2
        .value_kind:     hidden_remainder_z
      - .offset:         136
        .size:           8
        .value_kind:     hidden_global_offset_x
      - .offset:         144
        .size:           8
        .value_kind:     hidden_global_offset_y
      - .offset:         152
        .size:           8
        .value_kind:     hidden_global_offset_z
      - .offset:         160
        .size:           2
        .value_kind:     hidden_grid_dims
      - .offset:         216
        .size:           4
        .value_kind:     hidden_dynamic_lds_size
    .group_segment_fixed_size: 256
    .kernarg_segment_align: 8
    .kernarg_segment_size: 352
    .language:       OpenCL C
    .language_version:
      - 2
      - 0
    .max_flat_workgroup_size: 1024
    .name:           _Z7k_layerILi1EEvPKDF16_PKiPKjS3_S3_S1_PKfPDF16_PhS3_S7_Pf
    .private_segment_fixed_size: 0
    .sgpr_count:     38
    .sgpr_spill_count: 0
    .symbol:         _Z7k_layerILi1EEvPKDF16_PKiPKjS3_S3_S1_PKfPDF16_PhS3_S7_Pf.kd
    .uniform_work_group_size: 1
    .uses_dynamic_stack: false
    .vgpr_count:     114
    .vgpr_spill_count: 0
    .wavefront_size: 64
  - .agpr_count:     0
    .args:
      - .actual_access:  read_only
        .address_space:  global
        .offset:         0
        .size:           8
        .value_kind:     global_buffer
      - .actual_access:  read_only
        .address_space:  global
        .offset:         8
        .size:           8
        .value_kind:     global_buffer
      - .actual_access:  read_only
        .address_space:  global
        .offset:         16
        .size:           8
        .value_kind:     global_buffer
      - .actual_access:  read_only
        .address_space:  global
        .offset:         24
        .size:           8
        .value_kind:     global_buffer
      - .actual_access:  read_only
        .address_space:  global
        .offset:         32
        .size:           8
        .value_kind:     global_buffer
      - .actual_access:  read_only
        .address_space:  global
        .offset:         40
        .size:           8
        .value_kind:     global_buffer
      - .address_space:  global
        .offset:         48
        .size:           8
        .value_kind:     global_buffer
      - .actual_access:  read_only
        .address_space:  global
        .offset:         56
        .size:           8
        .value_kind:     global_buffer
      - .address_space:  global
        .offset:         64
        .size:           8
        .value_kind:     global_buffer
      - .actual_access:  read_only
        .address_space:  global
        .offset:         72
        .size:           8
        .value_kind:     global_buffer
      - .address_space:  global
        .offset:         80
        .size:           8
        .value_kind:     global_buffer
      - .address_space:  global
        .offset:         88
        .size:           8
        .value_kind:     global_buffer
      - .offset:         96
        .size:           4
        .value_kind:     hidden_block_count_x
      - .offset:         100
        .size:           4
        .value_kind:     hidden_block_count_y
      - .offset:         104
        .size:           4
        .value_kind:     hidden_block_count_z
      - .offset:         108
        .size:           2
        .value_kind:     hidden_group_size_x
      - .offset:         110
        .size:           2
        .value_kind:     hidden_group_size_y
      - .offset:         112
        .size:           2
        .value_kind:     hidden_group_size_z
      - .offset:         114
        .size:           2
        .value_kind:     hidden_remainder_x
      - .offset:         116
        .size:           2
        .value_kind:     hidden_remainder_y
      - .offset:         118
        .size:           2
        .value_kind:     hidden_remainder_z
      - .offset:         136
        .size:           8
        .value_kind:     hidden_global_offset_x
      - .offset:         144
        .size:           8
        .value_kind:     hidden_global_offset_y
      - .offset:         152
        .size:           8
        .value_kind:     hidden_global_offset_z
      - .offset:         160
        .size:           2
        .value_kind:     hidden_grid_dims
      - .offset:         216
        .size:           4
        .value_kind:     hidden_dynamic_lds_size
    .group_segment_fixed_size: 768
    .kernarg_segment_align: 8
    .kernarg_segment_size: 352
    .language:       OpenCL C
    .language_version:
      - 2
      - 0
    .max_flat_workgroup_size: 1024
    .name:           _Z7k_layerILi2EEvPKDF16_PKiPKjS3_S3_S1_PKfPDF16_PhS3_S7_Pf
    .private_segment_fixed_size: 0
    .sgpr_count:     44
    .sgpr_spill_count: 0
    .symbol:         _Z7k_layerILi2EEvPKDF16_PKiPKjS3_S3_S1_PKfPDF16_PhS3_S7_Pf.kd
    .uniform_work_group_size: 1
    .uses_dynamic_stack: false
    .vgpr_count:     102
    .vgpr_spill_count: 0
    .wavefront_size: 64
